# P8: B half-tile rows permuted so each wave owns 64 contiguous output columns; epilogue stores 16 rows x 64B per instruction
# speedup vs baseline: 1.0268x; 1.0033x over previous
.LBB0_991:
	v_bfe_u32 v2, v178, 2, 4
	v_lshrrev_b32_e32 v3, 3, v178
	s_movk_i32 s7, 0x70
	v_lshlrev_b32_e32 v0, 4, v178
	v_and_b32_e32 v1, 32, v178
	v_and_or_b32 v3, v3, s7, v2
	v_bitop3_b32 v1, v0, v1, 48 bitop3:0x6c
	s_waitcnt vmcnt(2)
	v_and_b32_e32 v4, 64, v178
	v_lshlrev_b32_e32 v3, 7, v3
	v_add_u32_e32 v0, 0x2000, v0
	v_or3_b32 v176, v3, v4, v1
	v_lshrrev_b32_e32 v3, 7, v0
	s_movk_i32 s7, 0xf0
	v_and_or_b32 v2, v3, s7, v2
	v_lshrrev_b32_e32 v0, 4, v0
	v_and_b32_e32 v0, 64, v0
	v_lshlrev_b32_e32 v2, 7, v2
	v_or3_b32 v180, v2, v0, v1
	v_and_b32_e32 v2, 0x1000, v176
	v_and_b32_e32 v3, 0x1000, v180
	v_add_u32_e32 v176, v176, v2
	v_add_u32_e32 v180, v180, v3
	v_add_u32_e32 v180, 0x3e000, v180
	v_mov_b32_e32 v0, v178
	s_lshr_b32 s14, s40, 6
	v_ashrrev_i32_e32 v2, 31, v0
	v_lshrrev_b32_e32 v2, 26, v2
	v_lshlrev_b32_e32 v1, 4, v0
	v_add_u32_e32 v2, v0, v2
	v_bfe_i32 v0, v0, 27, 1
	v_lshrrev_b32_e32 v0, 22, v0
	v_add_u32_e32 v0, v1, v0
	v_and_b32_e32 v0, 0xfffffc00, v0
	v_sub_u32_e32 v0, v1, v0
	v_lshrrev_b32_e32 v3, 4, v0
	v_bitop3_b32 v0, v3, v0, 32 bitop3:0x6c
	v_ashrrev_i32_e32 v4, 31, v0
	v_lshrrev_b32_e32 v4, 26, v4
	v_add_u32_e32 v4, v0, v4
	s_lshr_b32 s11, s40, 8
	s_lshl_b32 s45, s14, 10
	v_ashrrev_i32_e32 v2, 6, v2
	v_lshrrev_b32_e32 v5, 6, v4
	v_and_b32_e32 v4, 0xc0, v4
	s_add_u32 s12, s90, 0xf1a0000
	v_lshlrev_b32_e32 v3, 3, v2
	v_lshlrev_b32_e32 v2, 5, v2
	v_sub_u32_e32 v0, v0, v4
	v_mov_b32_e32 v192, 1
	s_addc_u32 s13, s91, 0
	s_lshl_b32 s7, s81, 11
	v_and_b32_e32 v3, 0x1fffff0, v3
	v_and_b32_e32 v2, 32, v2
	v_ashrrev_i16_sdwa v0, v192, sext(v0) dst_sel:DWORD dst_unused:UNUSED_PAD src0_sel:DWORD src1_sel:BYTE_0
	s_and_b32 s7, s7, 0xfffc0000
	v_add_u32_sdwa v0, v2, sext(v0) dst_sel:DWORD dst_unused:UNUSED_PAD src0_sel:DWORD src1_sel:WORD_0
	v_add_lshl_u32 v2, v5, v3, 7
	v_lshl_add_u32 v0, v0, 1, v2
	s_add_i32 s15, s7, 0x40000
	v_add_u32_e32 v184, s7, v0
	v_add_u32_e32 v182, s15, v0
	v_add_u32_e32 v0, 0x2000, v1
	v_ashrrev_i32_e32 v1, 31, v0
	v_lshrrev_b32_e32 v1, 22, v1
	v_add_u32_e32 v1, v0, v1
	v_ashrrev_i32_e32 v1, 10, v1
	v_mul_i32_i24_e32 v2, 0x400, v1
	v_sub_u32_e32 v0, v0, v2
	v_lshrrev_b32_e32 v2, 4, v0
	v_bitop3_b32 v0, v2, v0, 32 bitop3:0x6c
	v_ashrrev_i32_e32 v3, 31, v0
	v_lshrrev_b32_e32 v3, 26, v3
	v_add_u32_e32 v3, v0, v3
	v_lshrrev_b32_e32 v4, 6, v3
	v_and_b32_e32 v3, 0xc0, v3
	v_lshlrev_b32_e32 v2, 3, v1
	v_lshlrev_b32_e32 v1, 5, v1
	v_sub_u32_e32 v0, v0, v3
	s_add_i32 s46, s45, 0x100
	v_and_b32_e32 v2, 0x1fffff0, v2
	v_and_b32_e32 v1, 32, v1
	v_ashrrev_i16_sdwa v0, v192, sext(v0) dst_sel:DWORD dst_unused:UNUSED_PAD src0_sel:DWORD src1_sel:BYTE_0
	s_mov_b32 m0, s46
	s_add_i32 s47, s46, 0x2000
	v_add_u32_sdwa v0, v1, sext(v0) dst_sel:DWORD dst_unused:UNUSED_PAD src0_sel:DWORD src1_sel:WORD_0
	v_add_lshl_u32 v1, v4, v2, 7
	global_load_lds_dwordx4 v176, s[8:9]
	s_mov_b32 m0, s47
	s_add_i32 s48, s46, 0x10000
	s_add_i32 s49, s46, 0x12000
	v_lshl_add_u32 v0, v0, 1, v1
	global_load_lds_dwordx4 v180, s[8:9]
	s_mov_b32 m0, s48
	s_add_u32 s16, s8, 0x1000
	v_add_u32_e32 v186, s7, v0
	global_load_lds_dwordx4 v184, s[12:13]
	s_mov_b32 m0, s49
	s_addc_u32 s17, s9, 0
	s_add_i32 s50, s46, 0x4000
	global_load_lds_dwordx4 v186, s[12:13]
	s_mov_b32 m0, s50
	s_add_i32 s51, s46, 0x6000
	global_load_lds_dwordx4 v176, s[16:17]
	s_mov_b32 m0, s51
	v_add_u32_e32 v188, s15, v0
	global_load_lds_dwordx4 v180, s[16:17]
	s_add_i32 m0, s46, 0x14000
	v_mov_b32_e32 v183, 0
	global_load_lds_dwordx4 v182, s[12:13]
	s_add_i32 m0, s46, 0x16000
	v_mov_b32_e32 v177, v183
	global_load_lds_dwordx4 v188, s[12:13]
	v_mov_b32_e32 v181, v183
	v_mov_b32_e32 v185, v183
	v_mov_b32_e32 v187, v183
	s_cmp_lg_u32 s11, 1
	s_mov_b32 s7, 0x14000
	s_cbranch_scc1 .LBB0_993
	s_barrier
.LBB0_993:
	v_bfe_u32 v2, v178, 4, 2
	v_and_b32_e32 v0, 15, v178
	v_lshlrev_b32_e32 v1, 4, v2
	v_lshlrev_b32_e32 v3, 2, v178
	v_lshl_or_b32 v193, s11, 6, v0
	v_lshl_or_b32 v0, v0, 6, v1
	s_lshl_b32 s11, s11, 13
	v_and_b32_e32 v3, 32, v3
	v_bitop3_b32 v194, v0, s11, v3 bitop3:0xde
	s_lshl_b32 s11, s14, 5
	s_and_b32 s14, s11, 0x60
	v_lshlrev_b32_e32 v0, 6, v178
	s_movk_i32 s11, 0x3c0
	v_and_or_b32 v0, v0, s11, v1
	s_lshl_b32 s11, s14, 7
	s_add_u32 s16, s90, 0x191a0000
	s_addc_u32 s17, s91, 0
	s_add_u32 s18, s8, 0x4000
	s_addc_u32 s19, s9, 0
	s_add_i32 s52, s46, 0x8000
	v_bitop3_b32 v3, s11, v0, v3 bitop3:0xf6
	v_lshl_add_u64 v[0:1], s[18:19], 0, v[176:177]
	s_mov_b32 m0, s52
	s_add_i32 s53, s46, 0xa000
	s_waitcnt vmcnt(4)
	s_barrier
	global_load_lds_dwordx4 v[0:1], off
	v_lshl_add_u64 v[0:1], s[18:19], 0, v[180:181]
	s_add_u32 s18, s90, 0xf1a4000
	s_mov_b32 m0, s53
	s_addc_u32 s19, s91, 0
	global_load_lds_dwordx4 v[0:1], off
	s_add_i32 m0, s46, 0x18000
	v_lshl_add_u64 v[0:1], s[18:19], 0, v[184:185]
	global_load_lds_dwordx4 v[0:1], off
	s_add_i32 m0, s46, 0x1a000
	v_lshl_add_u64 v[0:1], s[18:19], 0, v[186:187]
	s_add_u32 s18, s8, 0x5000
	s_addc_u32 s19, s9, 0
	s_add_i32 s54, s46, 0xc000
	global_load_lds_dwordx4 v[0:1], off
	v_lshl_add_u64 v[0:1], s[18:19], 0, v[176:177]
	s_mov_b32 m0, s54
	s_add_i32 s55, s46, 0xe000
	global_load_lds_dwordx4 v[0:1], off
	v_lshl_add_u64 v[0:1], s[18:19], 0, v[180:181]
	s_mov_b32 m0, s55
	s_ashr_i32 s18, s33, 31
	global_load_lds_dwordx4 v[0:1], off
	s_lshr_b32 s18, s18, 29
	s_add_i32 s18, s33, s18
	s_ashr_i32 s19, s18, 3
	s_and_b32 s18, s18, -8
	s_sub_i32 s18, s33, s18
	s_ashr_i32 s20, s96, 3
	s_mul_i32 s18, s20, s18
	s_add_i32 s20, s18, s19
	s_cmp_lt_i32 s36, 24
	s_cselect_b64 s[18:19], -1, 0
	s_and_b64 s[2:3], s[2:3], exec
	s_mov_b32 s2, 0x20944
	s_cselect_b32 s56, s20, s33
	s_add_i32 s57, s2, 0x100
	s_mov_b32 s2, 0x20948
	s_add_i32 s58, s2, 0x100
	s_mov_b32 s2, 0x2094c
	s_add_i32 s59, s2, 0x100
	s_mov_b32 s2, 0x20950
	s_add_i32 s60, s2, 0x100
	s_mov_b32 s2, 0x20954
	s_add_i32 s61, s2, 0x100
	s_mov_b32 s2, 0x20958
	s_add_i32 s62, s2, 0x100
	s_mov_b32 s2, 0x2095c
	s_add_i32 s63, s2, 0x100
	s_mov_b32 s2, 0x20960
	s_add_i32 s64, s2, 0x100
	s_mov_b32 s2, 0x20964
	s_add_i32 s65, s2, 0x100
	s_mov_b32 s2, 0x20968
	s_add_i32 s68, s2, 0x100
	s_mov_b32 s2, 0x2096c
	s_add_i32 s69, s2, 0x100
	s_mov_b32 s2, 0x20970
	s_add_i32 s70, s2, 0x100
	s_mov_b32 s2, 0x20974
	s_addk_i32 s2, 0x100
	v_writelane_b32 v250, s2, 4
	s_mov_b32 s2, 0x20978
	s_addk_i32 s2, 0x100
	v_writelane_b32 v250, s2, 3
	s_mov_b32 s2, 0x2097c
	s_addk_i32 s2, 0x100
	v_writelane_b32 v250, s2, 5
	s_mov_b32 s2, 0x20980
	s_addk_i32 s2, 0x100
	v_writelane_b32 v250, s2, 6
	s_mov_b32 s2, 0x20984
	s_addk_i32 s2, 0x100
	v_writelane_b32 v250, s2, 7
	s_mov_b32 s2, 0x20988
	s_addk_i32 s2, 0x100
	v_writelane_b32 v250, s2, 8
	s_mov_b32 s2, 0x2098c
	s_addk_i32 s2, 0x100
	v_writelane_b32 v250, s2, 9
	s_mov_b32 s2, 0x20990
	s_addk_i32 s2, 0x100
	v_writelane_b32 v250, s2, 10
	s_mov_b32 s2, 0x20994
	s_addk_i32 s2, 0x100
	v_writelane_b32 v250, s2, 11
	s_mov_b32 s2, 0x20998
	s_addk_i32 s2, 0x100
	v_writelane_b32 v250, s2, 12
	s_mov_b32 s2, 0x2099c
	s_addk_i32 s2, 0x100
	v_writelane_b32 v250, s2, 13
	s_mov_b32 s2, 0x209a0
	s_addk_i32 s2, 0x100
	v_writelane_b32 v250, s2, 14
	s_mov_b32 s2, 0x209a4
	s_addk_i32 s2, 0x100
	v_writelane_b32 v250, s2, 15
	s_mov_b32 s2, 0x209a8
	s_add_i32 s84, s2, 0x100
	s_mov_b32 s2, 0x209ac
	s_add_i32 s85, s2, 0x100
	s_mov_b32 s2, 0x209b0
	s_add_i32 s97, s2, 0x100
	s_mov_b32 s2, 0x209b4
	s_waitcnt vmcnt(6)
	s_add_i32 s74, s2, 0x100
	s_mov_b32 s2, 0x209b8
	s_mov_b32 s11, 0x18000
	s_mov_b32 s15, 0
	v_lshlrev_b32_e32 v190, 2, v2
	s_add_i32 s73, s2, 0x100
	s_mov_b32 s2, 0x209bc
	v_mov_b32_e32 v191, v183
	v_or_b32_e32 v185, 16, v193
	v_or_b32_e32 v187, 32, v193
	v_or_b32_e32 v195, 48, v193
	s_add_i32 s75, s2, 0x100
	v_mov_b32_e32 v196, 0x7f7f7f7f
	v_mov_b32_e32 v197, 0x79797979
	s_add_i32 s76, s7, 0x100
	s_lshl_b32 s72, s14, 2
	v_lshlrev_b32_e32 v198, 2, v190
	s_mov_b32 s77, 0xc3e00000
	v_add_u32_e32 v199, 0x100, v3
	s_add_i32 s78, s11, 0x100
	v_mov_b32_e32 v200, 0x43e00000
	s_mov_b32 s44, s81
	s_mov_b32 s80, s15
	v_mov_b32_e32 v48, v183
	v_mov_b32_e32 v49, v183
	v_mov_b32_e32 v50, v183
	v_mov_b32_e32 v51, v183
	v_mov_b32_e32 v52, v183
	v_mov_b32_e32 v53, v183
	v_mov_b32_e32 v54, v183
	v_mov_b32_e32 v55, v183
	s_waitcnt vmcnt(0)
	v_mov_b32_e32 v56, v183
	v_mov_b32_e32 v57, v183
	v_mov_b32_e32 v58, v183
	v_mov_b32_e32 v59, v183
	v_mov_b32_e32 v60, v183
	v_mov_b32_e32 v61, v183
	v_mov_b32_e32 v62, v183
	v_mov_b32_e32 v63, v183
	v_mov_b32_e32 v64, v183
	v_mov_b32_e32 v65, v183
	v_mov_b32_e32 v66, v183
	v_mov_b32_e32 v67, v183
	v_mov_b32_e32 v68, v183
	v_mov_b32_e32 v69, v183
	v_mov_b32_e32 v70, v183
	v_mov_b32_e32 v71, v183
	v_mov_b32_e32 v72, v183
	v_mov_b32_e32 v73, v183
	v_mov_b32_e32 v74, v183
	v_mov_b32_e32 v75, v183
	v_mov_b32_e32 v76, v183
	v_mov_b32_e32 v77, v183
	v_mov_b32_e32 v78, v183
	v_mov_b32_e32 v79, v183
	v_mov_b32_e32 v80, v183
	v_mov_b32_e32 v81, v183
	v_mov_b32_e32 v82, v183
	v_mov_b32_e32 v83, v183
	v_mov_b32_e32 v84, v183
	v_mov_b32_e32 v85, v183
	v_mov_b32_e32 v86, v183
	v_mov_b32_e32 v87, v183
	v_mov_b32_e32 v88, v183
	v_mov_b32_e32 v89, v183
	v_mov_b32_e32 v90, v183
	v_mov_b32_e32 v91, v183
	v_mov_b32_e32 v92, v183
	v_mov_b32_e32 v93, v183
	v_mov_b32_e32 v94, v183
	v_mov_b32_e32 v95, v183
	v_mov_b32_e32 v96, v183
	v_mov_b32_e32 v97, v183
	v_mov_b32_e32 v98, v183
	v_mov_b32_e32 v99, v183
	v_mov_b32_e32 v100, v183
	v_mov_b32_e32 v101, v183
	v_mov_b32_e32 v102, v183
	v_mov_b32_e32 v103, v183
	v_mov_b32_e32 v104, v183
	v_mov_b32_e32 v105, v183
	v_mov_b32_e32 v106, v183
	v_mov_b32_e32 v107, v183
	v_mov_b32_e32 v108, v183
	v_mov_b32_e32 v109, v183
	v_mov_b32_e32 v110, v183
	v_mov_b32_e32 v111, v183
	v_mov_b32_e32 v112, v183
	v_mov_b32_e32 v113, v183
	v_mov_b32_e32 v114, v183
	v_mov_b32_e32 v115, v183
	v_mov_b32_e32 v116, v183
	v_mov_b32_e32 v117, v183
	v_mov_b32_e32 v118, v183
	v_mov_b32_e32 v119, v183
	v_mov_b32_e32 v120, v183
	v_mov_b32_e32 v121, v183
	v_mov_b32_e32 v122, v183
	v_mov_b32_e32 v123, v183
	v_mov_b32_e32 v124, v183
	v_mov_b32_e32 v125, v183
	v_mov_b32_e32 v126, v183
	v_mov_b32_e32 v127, v183
	v_mov_b32_e32 v128, v183
	v_mov_b32_e32 v129, v183
	v_mov_b32_e32 v130, v183
	v_mov_b32_e32 v131, v183
	v_mov_b32_e32 v132, v183
	v_mov_b32_e32 v133, v183
	v_mov_b32_e32 v134, v183
	v_mov_b32_e32 v135, v183
	v_mov_b32_e32 v136, v183
	v_mov_b32_e32 v137, v183
	v_mov_b32_e32 v138, v183
	v_mov_b32_e32 v139, v183
	v_mov_b32_e32 v140, v183
	v_mov_b32_e32 v141, v183
	v_mov_b32_e32 v142, v183
	v_mov_b32_e32 v143, v183
	v_mov_b32_e32 v144, v183
	v_mov_b32_e32 v145, v183
	v_mov_b32_e32 v146, v183
	v_mov_b32_e32 v147, v183
	v_mov_b32_e32 v148, v183
	v_mov_b32_e32 v149, v183
	v_mov_b32_e32 v150, v183
	v_mov_b32_e32 v151, v183
	v_mov_b32_e32 v152, v183
	v_mov_b32_e32 v153, v183
	v_mov_b32_e32 v154, v183
	v_mov_b32_e32 v155, v183
	v_mov_b32_e32 v156, v183
	v_mov_b32_e32 v157, v183
	v_mov_b32_e32 v158, v183
	v_mov_b32_e32 v159, v183
	v_mov_b32_e32 v160, v183
	v_mov_b32_e32 v161, v183
	v_mov_b32_e32 v162, v183
	v_mov_b32_e32 v163, v183
	v_mov_b32_e32 v164, v183
	v_mov_b32_e32 v165, v183
	v_mov_b32_e32 v166, v183
	v_mov_b32_e32 v167, v183
	v_mov_b32_e32 v168, v183
	v_mov_b32_e32 v169, v183
	v_mov_b32_e32 v170, v183
	v_mov_b32_e32 v171, v183
	v_mov_b32_e32 v172, v183
	v_mov_b32_e32 v173, v183
	v_mov_b32_e32 v174, v183
	v_mov_b32_e32 v175, v183
	s_barrier
	s_branch .LBB0_995

.LBB0_1044:
	s_add_u32 s34, s26, 0xf0e64000
	s_addc_u32 s35, s27, -1
	s_and_b64 s[30:31], s[28:29], exec
	s_cselect_b32 s31, 0, s34
	s_cselect_b32 s30, 0, s35
	s_add_u32 s36, s12, s31
	s_addc_u32 s37, s13, s30
	s_add_u32 s30, s8, s26
	s_addc_u32 s31, s9, s27
	s_add_u32 s30, s30, 0xf0e64000
	s_addc_u32 s31, s31, -1
	s_and_b64 s[28:29], s[28:29], exec
	s_cselect_b32 s29, s23, s31
	s_cselect_b32 s28, s22, s30
	s_add_u32 s30, s36, 0x4000
	s_waitcnt lgkmcnt(8)
	s_barrier
	s_waitcnt lgkmcnt(0)
	s_addc_u32 s31, s37, 0
	s_add_u32 s34, s28, 0x4000
	v_mov_b32_e32 v189, v183
	s_addc_u32 s35, s29, 0
	s_setprio 1
	s_waitcnt lgkmcnt(0)
	v_mfma_scale_f32_16x16x128_f8f6f4 v[172:175], v[0:7], v[40:47], v[172:175], v197, v196 op_sel_hi:[0,0,0]
	v_mfma_scale_f32_16x16x128_f8f6f4 v[168:171], v[8:15], v[40:47], v[168:171], v197, v196 op_sel_hi:[0,0,0]
	v_mfma_scale_f32_16x16x128_f8f6f4 v[164:167], v[0:7], v[32:39], v[164:167], v197, v196 op_sel_hi:[0,0,0]
	v_mfma_scale_f32_16x16x128_f8f6f4 v[160:163], v[8:15], v[32:39], v[160:163], v197, v196 op_sel_hi:[0,0,0]
	v_mfma_scale_f32_16x16x128_f8f6f4 v[202:205], v[0:7], v[24:31], v[156:159], v197, v196 op_sel_hi:[0,0,0]
	v_mfma_scale_f32_16x16x128_f8f6f4 v[206:209], v[8:15], v[24:31], v[152:155], v197, v196 op_sel_hi:[0,0,0]
	v_mfma_scale_f32_16x16x128_f8f6f4 v[210:213], v[0:7], v[16:23], v[148:151], v197, v196 op_sel_hi:[0,0,0]
	v_mfma_scale_f32_16x16x128_f8f6f4 v[214:217], v[8:15], v[16:23], v[144:147], v197, v196 op_sel_hi:[0,0,0]
	s_setprio 0
	s_barrier
	s_mov_b32 m0, s46
	v_lshl_add_u64 v[218:219], s[28:29], 0, v[176:177]
	s_nop 2
	ds_read_b128 v[144:147], v199 offset:16384
	ds_read_b128 v[148:151], v199 offset:17408
	ds_read_b128 v[152:155], v199 offset:18432
	ds_read_b128 v[156:159], v199 offset:19456
	global_load_lds_dwordx4 v[218:219], off
	v_lshl_add_u64 v[218:219], s[28:29], 0, v[180:181]
	s_mov_b32 m0, s47
	s_nop 0
	global_load_lds_dwordx4 v[218:219], off
	s_barrier
	s_waitcnt lgkmcnt(0)
	s_setprio 1
	s_waitcnt lgkmcnt(0)
	v_mfma_scale_f32_16x16x128_f8f6f4 v[140:143], v[144:151], v[40:47], v[140:143], v197, v196 op_sel_hi:[0,0,0]
	v_mfma_scale_f32_16x16x128_f8f6f4 v[136:139], v[152:159], v[40:47], v[136:139], v197, v196 op_sel_hi:[0,0,0]
	v_mfma_scale_f32_16x16x128_f8f6f4 v[132:135], v[144:151], v[32:39], v[132:135], v197, v196 op_sel_hi:[0,0,0]
	v_mfma_scale_f32_16x16x128_f8f6f4 v[128:131], v[152:159], v[32:39], v[128:131], v197, v196 op_sel_hi:[0,0,0]
	v_mfma_scale_f32_16x16x128_f8f6f4 v[124:127], v[144:151], v[24:31], v[124:127], v197, v196 op_sel_hi:[0,0,0]
	v_mfma_scale_f32_16x16x128_f8f6f4 v[120:123], v[152:159], v[24:31], v[120:123], v197, v196 op_sel_hi:[0,0,0]
	v_mfma_scale_f32_16x16x128_f8f6f4 v[116:119], v[144:151], v[16:23], v[116:119], v197, v196 op_sel_hi:[0,0,0]
	v_mfma_scale_f32_16x16x128_f8f6f4 v[112:115], v[152:159], v[16:23], v[112:115], v197, v196 op_sel_hi:[0,0,0]
	s_setprio 0
	v_add_u32_e32 v44, s76, v194
	s_mov_b32 m0, s48
	s_barrier
	ds_read_b128 v[16:19], v44
	ds_read_b128 v[20:23], v44 offset:1024
	ds_read_b128 v[24:27], v44 offset:2048
	ds_read_b128 v[28:31], v44 offset:3072
	ds_read_b128 v[32:35], v44 offset:4096
	ds_read_b128 v[36:39], v44 offset:5120
	ds_read_b128 v[40:43], v44 offset:6144
	ds_read_b128 v[44:47], v44 offset:7168
	global_load_lds_dwordx4 v184, s[36:37]
	s_mov_b32 m0, s49
	s_nop 0
	global_load_lds_dwordx4 v186, s[36:37]
	s_barrier
	s_waitcnt lgkmcnt(0)
	s_setprio 1
	s_waitcnt lgkmcnt(0)
	v_mfma_scale_f32_16x16x128_f8f6f4 v[108:111], v[0:7], v[16:23], v[108:111], v197, v196 op_sel_hi:[0,0,0]
	v_mfma_scale_f32_16x16x128_f8f6f4 v[104:107], v[8:15], v[16:23], v[104:107], v197, v196 op_sel_hi:[0,0,0]
	v_mfma_scale_f32_16x16x128_f8f6f4 v[100:103], v[0:7], v[24:31], v[100:103], v197, v196 op_sel_hi:[0,0,0]
	v_mfma_scale_f32_16x16x128_f8f6f4 v[96:99], v[8:15], v[24:31], v[96:99], v197, v196 op_sel_hi:[0,0,0]
	v_mfma_scale_f32_16x16x128_f8f6f4 v[92:95], v[0:7], v[32:39], v[92:95], v197, v196 op_sel_hi:[0,0,0]
	v_mfma_scale_f32_16x16x128_f8f6f4 v[88:91], v[8:15], v[32:39], v[88:91], v197, v196 op_sel_hi:[0,0,0]
	v_mfma_scale_f32_16x16x128_f8f6f4 v[84:87], v[0:7], v[40:47], v[84:87], v197, v196 op_sel_hi:[0,0,0]
	v_mfma_scale_f32_16x16x128_f8f6f4 v[80:83], v[8:15], v[40:47], v[80:83], v197, v196 op_sel_hi:[0,0,0]
	s_setprio 0
	s_barrier
	s_add_u32 vcc_lo, s28, 0x1000
	s_addc_u32 vcc_hi, s29, 0
	s_mov_b32 m0, s50
	v_lshl_add_u64 v[0:1], vcc, 0, v[176:177]
	global_load_lds_dwordx4 v[0:1], off
	v_lshl_add_u64 v[0:1], vcc, 0, v[180:181]
	s_mov_b32 m0, s51
	s_nop 0
	global_load_lds_dwordx4 v[0:1], off
	s_waitcnt vmcnt(6)
	s_barrier
	s_setprio 1
	v_mfma_scale_f32_16x16x128_f8f6f4 v[76:79], v[144:151], v[16:23], v[76:79], v197, v196 op_sel_hi:[0,0,0]
	v_mfma_scale_f32_16x16x128_f8f6f4 v[72:75], v[152:159], v[16:23], v[72:75], v197, v196 op_sel_hi:[0,0,0]
	v_mfma_scale_f32_16x16x128_f8f6f4 v[68:71], v[144:151], v[24:31], v[68:71], v197, v196 op_sel_hi:[0,0,0]
	v_mfma_scale_f32_16x16x128_f8f6f4 v[64:67], v[152:159], v[24:31], v[64:67], v197, v196 op_sel_hi:[0,0,0]
	v_mfma_scale_f32_16x16x128_f8f6f4 v[60:63], v[144:151], v[32:39], v[60:63], v197, v196 op_sel_hi:[0,0,0]
	v_mfma_scale_f32_16x16x128_f8f6f4 v[56:59], v[152:159], v[32:39], v[56:59], v197, v196 op_sel_hi:[0,0,0]
	v_mfma_scale_f32_16x16x128_f8f6f4 v[218:221], v[144:151], v[40:47], v[52:55], v197, v196 op_sel_hi:[0,0,0]
	v_mfma_scale_f32_16x16x128_f8f6f4 v[222:225], v[152:159], v[40:47], v[48:51], v197, v196 op_sel_hi:[0,0,0]
	s_setprio 0
	s_barrier
	ds_read_b128 v[0:3], v199 offset:32768
	ds_read_b128 v[4:7], v199 offset:33792
	ds_read_b128 v[8:11], v199 offset:34816
	ds_read_b128 v[12:15], v199 offset:35840
	s_add_i32 vcc_lo, s76, s45
	v_add_u32_e32 v44, s78, v194
	v_lshl_add_u64 v[48:49], s[36:37], 0, v[182:183]
	s_mov_b32 m0, vcc_lo
	ds_read_b128 v[16:19], v44
	ds_read_b128 v[20:23], v44 offset:1024
	ds_read_b128 v[24:27], v44 offset:2048
	ds_read_b128 v[28:31], v44 offset:3072
	ds_read_b128 v[32:35], v44 offset:4096
	ds_read_b128 v[36:39], v44 offset:5120
	ds_read_b128 v[40:43], v44 offset:6144
	ds_read_b128 v[44:47], v44 offset:7168
	global_load_lds_dwordx4 v[48:49], off
	v_lshl_add_u64 v[48:49], s[36:37], 0, v[188:189]
	s_add_i32 m0, vcc_lo, 0x2000
	s_nop 0
	global_load_lds_dwordx4 v[48:49], off
	s_waitcnt lgkmcnt(8)
	s_barrier
	s_waitcnt lgkmcnt(0)
	s_setprio 1
	s_waitcnt lgkmcnt(0)
	v_mfma_scale_f32_16x16x128_f8f6f4 v[172:175], v[0:7], v[16:23], v[172:175], v197, v196 op_sel_hi:[0,0,0]
	v_mfma_scale_f32_16x16x128_f8f6f4 v[168:171], v[8:15], v[16:23], v[168:171], v197, v196 op_sel_hi:[0,0,0]
	v_mfma_scale_f32_16x16x128_f8f6f4 v[164:167], v[0:7], v[24:31], v[164:167], v197, v196 op_sel_hi:[0,0,0]
	v_mfma_scale_f32_16x16x128_f8f6f4 v[160:163], v[8:15], v[24:31], v[160:163], v197, v196 op_sel_hi:[0,0,0]
	v_mfma_scale_f32_16x16x128_f8f6f4 v[156:159], v[0:7], v[32:39], v[202:205], v197, v196 op_sel_hi:[0,0,0]
	v_mfma_scale_f32_16x16x128_f8f6f4 v[152:155], v[8:15], v[32:39], v[206:209], v197, v196 op_sel_hi:[0,0,0]
	v_mfma_scale_f32_16x16x128_f8f6f4 v[148:151], v[0:7], v[40:47], v[210:213], v197, v196 op_sel_hi:[0,0,0]
	v_mfma_scale_f32_16x16x128_f8f6f4 v[144:147], v[8:15], v[40:47], v[214:217], v197, v196 op_sel_hi:[0,0,0]
	s_setprio 0
	s_barrier
	s_mov_b32 m0, s52
	s_nop 2
	v_lshl_add_u64 v[210:211], s[34:35], 0, v[176:177]
	ds_read_b128 v[48:51], v199 offset:49152
	ds_read_b128 v[52:55], v199 offset:50176
	ds_read_b128 v[202:205], v199 offset:51200
	ds_read_b128 v[206:209], v199 offset:52224
	global_load_lds_dwordx4 v[210:211], off
	v_lshl_add_u64 v[210:211], s[34:35], 0, v[180:181]
	s_mov_b32 m0, s53
	s_nop 0
	global_load_lds_dwordx4 v[210:211], off
	s_barrier
	s_waitcnt lgkmcnt(0)
	s_setprio 1
	s_waitcnt lgkmcnt(0)
	v_mfma_scale_f32_16x16x128_f8f6f4 v[140:143], v[48:55], v[16:23], v[140:143], v197, v196 op_sel_hi:[0,0,0]
	v_mfma_scale_f32_16x16x128_f8f6f4 v[136:139], v[202:209], v[16:23], v[136:139], v197, v196 op_sel_hi:[0,0,0]
	v_mfma_scale_f32_16x16x128_f8f6f4 v[132:135], v[48:55], v[24:31], v[132:135], v197, v196 op_sel_hi:[0,0,0]
	v_mfma_scale_f32_16x16x128_f8f6f4 v[128:131], v[202:209], v[24:31], v[128:131], v197, v196 op_sel_hi:[0,0,0]
	v_mfma_scale_f32_16x16x128_f8f6f4 v[124:127], v[48:55], v[32:39], v[124:127], v197, v196 op_sel_hi:[0,0,0]
	v_mfma_scale_f32_16x16x128_f8f6f4 v[120:123], v[202:209], v[32:39], v[120:123], v197, v196 op_sel_hi:[0,0,0]
	v_mfma_scale_f32_16x16x128_f8f6f4 v[116:119], v[48:55], v[40:47], v[116:119], v197, v196 op_sel_hi:[0,0,0]
	v_mfma_scale_f32_16x16x128_f8f6f4 v[112:115], v[202:209], v[40:47], v[112:115], v197, v196 op_sel_hi:[0,0,0]
	s_setprio 0
	s_add_i32 s34, s78, s45
	v_add_u32_e32 v44, 0x1c000, v201
	s_mov_b32 m0, s34
	s_barrier
	ds_read_b128 v[16:19], v44
	ds_read_b128 v[20:23], v44 offset:1024
	ds_read_b128 v[24:27], v44 offset:2048
	ds_read_b128 v[28:31], v44 offset:3072
	ds_read_b128 v[32:35], v44 offset:4096
	ds_read_b128 v[36:39], v44 offset:5120
	ds_read_b128 v[40:43], v44 offset:6144
	ds_read_b128 v[44:47], v44 offset:7168
	global_load_lds_dwordx4 v184, s[30:31]
	s_add_i32 m0, s34, 0x2000
	s_nop 0
	global_load_lds_dwordx4 v186, s[30:31]
	s_barrier
	s_waitcnt lgkmcnt(0)
	s_setprio 1
	s_waitcnt lgkmcnt(0)
	v_mfma_scale_f32_16x16x128_f8f6f4 v[108:111], v[0:7], v[16:23], v[108:111], v197, v196 op_sel_hi:[0,0,0]
	v_mfma_scale_f32_16x16x128_f8f6f4 v[104:107], v[8:15], v[16:23], v[104:107], v197, v196 op_sel_hi:[0,0,0]
	v_mfma_scale_f32_16x16x128_f8f6f4 v[100:103], v[0:7], v[24:31], v[100:103], v197, v196 op_sel_hi:[0,0,0]
	v_mfma_scale_f32_16x16x128_f8f6f4 v[96:99], v[8:15], v[24:31], v[96:99], v197, v196 op_sel_hi:[0,0,0]
	v_mfma_scale_f32_16x16x128_f8f6f4 v[92:95], v[0:7], v[32:39], v[92:95], v197, v196 op_sel_hi:[0,0,0]
	v_mfma_scale_f32_16x16x128_f8f6f4 v[88:91], v[8:15], v[32:39], v[88:91], v197, v196 op_sel_hi:[0,0,0]
	v_mfma_scale_f32_16x16x128_f8f6f4 v[84:87], v[0:7], v[40:47], v[84:87], v197, v196 op_sel_hi:[0,0,0]
	v_mfma_scale_f32_16x16x128_f8f6f4 v[80:83], v[8:15], v[40:47], v[80:83], v197, v196 op_sel_hi:[0,0,0]
	s_setprio 0
	s_barrier
	s_add_u32 s28, s28, 0x5000
	s_addc_u32 s29, s29, 0
	s_mov_b32 m0, s54
	v_lshl_add_u64 v[0:1], s[28:29], 0, v[176:177]
	global_load_lds_dwordx4 v[0:1], off
	v_lshl_add_u64 v[0:1], s[28:29], 0, v[180:181]
	s_mov_b32 m0, s55
	s_nop 0
	global_load_lds_dwordx4 v[0:1], off
	s_waitcnt vmcnt(6)
	s_barrier
	s_setprio 1
	v_mfma_scale_f32_16x16x128_f8f6f4 v[76:79], v[48:55], v[16:23], v[76:79], v197, v196 op_sel_hi:[0,0,0]
	v_mfma_scale_f32_16x16x128_f8f6f4 v[72:75], v[202:209], v[16:23], v[72:75], v197, v196 op_sel_hi:[0,0,0]
	v_mfma_scale_f32_16x16x128_f8f6f4 v[68:71], v[48:55], v[24:31], v[68:71], v197, v196 op_sel_hi:[0,0,0]
	v_mfma_scale_f32_16x16x128_f8f6f4 v[64:67], v[202:209], v[24:31], v[64:67], v197, v196 op_sel_hi:[0,0,0]
	v_mfma_scale_f32_16x16x128_f8f6f4 v[60:63], v[48:55], v[32:39], v[60:63], v197, v196 op_sel_hi:[0,0,0]
	v_mfma_scale_f32_16x16x128_f8f6f4 v[56:59], v[202:209], v[32:39], v[56:59], v197, v196 op_sel_hi:[0,0,0]
	v_mfma_scale_f32_16x16x128_f8f6f4 v[52:55], v[48:55], v[40:47], v[218:221], v197, v196 op_sel_hi:[0,0,0]
	v_mfma_scale_f32_16x16x128_f8f6f4 v[48:51], v[202:209], v[40:47], v[222:225], v197, v196 op_sel_hi:[0,0,0]
	s_setprio 0
	s_add_i32 s83, s83, 2
	s_add_u32 s26, s26, 0x8000
	s_addc_u32 s27, s27, 0
	s_cmp_gt_u32 s83, 13
	s_barrier
	s_cbranch_scc1 .LBB0_1047

.LBB0_1047:
	s_ashr_i32 s7, s6, 31
	s_lshl_b64 s[26:27], s[6:7], 13
	s_add_u32 s7, s86, s26
	s_addc_u32 s28, s87, s27
	s_ashr_i32 s11, s10, 31
	s_lshl_b64 s[26:27], s[10:11], 2
	s_add_u32 s7, s7, s26
	s_addc_u32 s27, s28, s27
	s_add_u32 s26, s7, s72
	s_addc_u32 s27, s27, 0
	s_add_u32 s26, s26, s72
	s_addc_u32 s27, s27, 0
	global_load_dwordx4 v[12:15], v198, s[26:27]
	global_load_dwordx4 v[8:11], v198, s[26:27] offset:64
	global_load_dwordx4 v[4:7], v198, s[26:27] offset:128
	global_load_dwordx4 v[0:3], v198, s[26:27] offset:192
	s_andn2_b64 vcc, exec, s[24:25]
	v_add_u32_e32 v16, s44, v193
	v_ashrrev_i32_e32 v17, 31, v16
	v_lshlrev_b64 v[252:253], 11, v[16:17]
	v_bfe_u32 v16, v178, 4, 2
	v_lshlrev_b32_e32 v16, 4, v16
	v_mov_b32_e32 v17, 0
	v_lshl_add_u64 v[252:253], s[16:17], 0, v[252:253]
	v_lshl_add_u64 v[252:253], v[252:253], 0, s[10:11]
	v_lshl_add_u64 v[252:253], v[252:253], 0, s[14:15]
	v_lshl_add_u64 v[252:253], v[252:253], 0, s[14:15]
	v_lshl_add_u64 v[252:253], v[252:253], 0, v[16:17]
	s_mov_b64 s[100:101], 0x8000
	s_waitcnt vmcnt(0)
	v_pk_add_f32 v[24:25], v[172:173], v[12:13]
	v_pk_add_f32 v[26:27], v[174:175], v[14:15]
	v_pk_add_f32 v[28:29], v[168:169], v[8:9]
	v_pk_add_f32 v[30:31], v[170:171], v[10:11]
	v_pk_add_f32 v[32:33], v[140:141], v[4:5]
	v_pk_add_f32 v[34:35], v[142:143], v[6:7]
	v_pk_add_f32 v[36:37], v[136:137], v[0:1]
	v_pk_add_f32 v[38:39], v[138:139], v[2:3]
	v_med3_f32 v24, v24, s77, v200
	v_med3_f32 v25, v25, s77, v200
	v_med3_f32 v26, v26, s77, v200
	v_med3_f32 v27, v27, s77, v200
	v_med3_f32 v28, v28, s77, v200
	v_med3_f32 v29, v29, s77, v200
	v_med3_f32 v30, v30, s77, v200
	v_med3_f32 v31, v31, s77, v200
	v_med3_f32 v32, v32, s77, v200
	v_med3_f32 v33, v33, s77, v200
	v_med3_f32 v34, v34, s77, v200
	v_med3_f32 v35, v35, s77, v200
	v_med3_f32 v36, v36, s77, v200
	v_med3_f32 v37, v37, s77, v200
	v_med3_f32 v38, v38, s77, v200
	v_med3_f32 v39, v39, s77, v200
	v_cvt_pk_fp8_f32 v20, v24, v25
	v_cvt_pk_fp8_f32 v21, v28, v29
	v_cvt_pk_fp8_f32 v22, v32, v33
	v_cvt_pk_fp8_f32 v23, v36, v37
	v_cvt_pk_fp8_f32 v20, v26, v27 op_sel:[0,0,1]
	v_cvt_pk_fp8_f32 v21, v30, v31 op_sel:[0,0,1]
	v_cvt_pk_fp8_f32 v22, v34, v35 op_sel:[0,0,1]
	v_cvt_pk_fp8_f32 v23, v38, v39 op_sel:[0,0,1]
	s_nop 1
	v_permlane32_swap_b32_e32 v20, v22
	v_permlane32_swap_b32_e32 v21, v23
	s_nop 1
	v_permlane16_swap_b32_e32 v20, v21
	v_permlane16_swap_b32_e32 v22, v23
	global_store_dwordx4 v[252:253], v[20:23], off
	v_lshl_add_u64 v[252:253], v[252:253], 0, s[100:101]
	v_pk_add_f32 v[24:25], v[164:165], v[12:13]
	v_pk_add_f32 v[26:27], v[166:167], v[14:15]
	v_pk_add_f32 v[28:29], v[160:161], v[8:9]
	v_pk_add_f32 v[30:31], v[162:163], v[10:11]
	v_pk_add_f32 v[32:33], v[132:133], v[4:5]
	v_pk_add_f32 v[34:35], v[134:135], v[6:7]
	v_pk_add_f32 v[36:37], v[128:129], v[0:1]
	v_pk_add_f32 v[38:39], v[130:131], v[2:3]
	v_med3_f32 v24, v24, s77, v200
	v_med3_f32 v25, v25, s77, v200
	v_med3_f32 v26, v26, s77, v200
	v_med3_f32 v27, v27, s77, v200
	v_med3_f32 v28, v28, s77, v200
	v_med3_f32 v29, v29, s77, v200
	v_med3_f32 v30, v30, s77, v200
	v_med3_f32 v31, v31, s77, v200
	v_med3_f32 v32, v32, s77, v200
	v_med3_f32 v33, v33, s77, v200
	v_med3_f32 v34, v34, s77, v200
	v_med3_f32 v35, v35, s77, v200
	v_med3_f32 v36, v36, s77, v200
	v_med3_f32 v37, v37, s77, v200
	v_med3_f32 v38, v38, s77, v200
	v_med3_f32 v39, v39, s77, v200
	v_cvt_pk_fp8_f32 v40, v24, v25
	v_cvt_pk_fp8_f32 v41, v28, v29
	v_cvt_pk_fp8_f32 v42, v32, v33
	v_cvt_pk_fp8_f32 v43, v36, v37
	v_cvt_pk_fp8_f32 v40, v26, v27 op_sel:[0,0,1]
	v_cvt_pk_fp8_f32 v41, v30, v31 op_sel:[0,0,1]
	v_cvt_pk_fp8_f32 v42, v34, v35 op_sel:[0,0,1]
	v_cvt_pk_fp8_f32 v43, v38, v39 op_sel:[0,0,1]
	s_nop 1
	v_permlane32_swap_b32_e32 v40, v42
	v_permlane32_swap_b32_e32 v41, v43
	s_nop 1
	v_permlane16_swap_b32_e32 v40, v41
	v_permlane16_swap_b32_e32 v42, v43
	global_store_dwordx4 v[252:253], v[40:43], off
	v_lshl_add_u64 v[252:253], v[252:253], 0, s[100:101]
	v_pk_add_f32 v[24:25], v[156:157], v[12:13]
	v_pk_add_f32 v[26:27], v[158:159], v[14:15]
	v_pk_add_f32 v[28:29], v[152:153], v[8:9]
	v_pk_add_f32 v[30:31], v[154:155], v[10:11]
	v_pk_add_f32 v[32:33], v[124:125], v[4:5]
	v_pk_add_f32 v[34:35], v[126:127], v[6:7]
	v_pk_add_f32 v[36:37], v[120:121], v[0:1]
	v_pk_add_f32 v[38:39], v[122:123], v[2:3]
	v_med3_f32 v24, v24, s77, v200
	v_med3_f32 v25, v25, s77, v200
	v_med3_f32 v26, v26, s77, v200
	v_med3_f32 v27, v27, s77, v200
	v_med3_f32 v28, v28, s77, v200
	v_med3_f32 v29, v29, s77, v200
	v_med3_f32 v30, v30, s77, v200
	v_med3_f32 v31, v31, s77, v200
	v_med3_f32 v32, v32, s77, v200
	v_med3_f32 v33, v33, s77, v200
	v_med3_f32 v34, v34, s77, v200
	v_med3_f32 v35, v35, s77, v200
	v_med3_f32 v36, v36, s77, v200
	v_med3_f32 v37, v37, s77, v200
	v_med3_f32 v38, v38, s77, v200
	v_med3_f32 v39, v39, s77, v200
	v_cvt_pk_fp8_f32 v20, v24, v25
	v_cvt_pk_fp8_f32 v21, v28, v29
	v_cvt_pk_fp8_f32 v22, v32, v33
	v_cvt_pk_fp8_f32 v23, v36, v37
	v_cvt_pk_fp8_f32 v20, v26, v27 op_sel:[0,0,1]
	v_cvt_pk_fp8_f32 v21, v30, v31 op_sel:[0,0,1]
	v_cvt_pk_fp8_f32 v22, v34, v35 op_sel:[0,0,1]
	v_cvt_pk_fp8_f32 v23, v38, v39 op_sel:[0,0,1]
	s_nop 1
	v_permlane32_swap_b32_e32 v20, v22
	v_permlane32_swap_b32_e32 v21, v23
	s_nop 1
	v_permlane16_swap_b32_e32 v20, v21
	v_permlane16_swap_b32_e32 v22, v23
	global_store_dwordx4 v[252:253], v[20:23], off
	v_lshl_add_u64 v[252:253], v[252:253], 0, s[100:101]
	v_pk_add_f32 v[24:25], v[148:149], v[12:13]
	v_pk_add_f32 v[26:27], v[150:151], v[14:15]
	v_pk_add_f32 v[28:29], v[144:145], v[8:9]
	v_pk_add_f32 v[30:31], v[146:147], v[10:11]
	v_pk_add_f32 v[32:33], v[116:117], v[4:5]
	v_pk_add_f32 v[34:35], v[118:119], v[6:7]
	v_pk_add_f32 v[36:37], v[112:113], v[0:1]
	v_pk_add_f32 v[38:39], v[114:115], v[2:3]
	v_med3_f32 v24, v24, s77, v200
	v_med3_f32 v25, v25, s77, v200
	v_med3_f32 v26, v26, s77, v200
	v_med3_f32 v27, v27, s77, v200
	v_med3_f32 v28, v28, s77, v200
	v_med3_f32 v29, v29, s77, v200
	v_med3_f32 v30, v30, s77, v200
	v_med3_f32 v31, v31, s77, v200
	v_med3_f32 v32, v32, s77, v200
	v_med3_f32 v33, v33, s77, v200
	v_med3_f32 v34, v34, s77, v200
	v_med3_f32 v35, v35, s77, v200
	v_med3_f32 v36, v36, s77, v200
	v_med3_f32 v37, v37, s77, v200
	v_med3_f32 v38, v38, s77, v200
	v_med3_f32 v39, v39, s77, v200
	v_cvt_pk_fp8_f32 v40, v24, v25
	v_cvt_pk_fp8_f32 v41, v28, v29
	v_cvt_pk_fp8_f32 v42, v32, v33
	v_cvt_pk_fp8_f32 v43, v36, v37
	v_cvt_pk_fp8_f32 v40, v26, v27 op_sel:[0,0,1]
	v_cvt_pk_fp8_f32 v41, v30, v31 op_sel:[0,0,1]
	v_cvt_pk_fp8_f32 v42, v34, v35 op_sel:[0,0,1]
	v_cvt_pk_fp8_f32 v43, v38, v39 op_sel:[0,0,1]
	s_nop 1
	v_permlane32_swap_b32_e32 v40, v42
	v_permlane32_swap_b32_e32 v41, v43
	s_nop 1
	v_permlane16_swap_b32_e32 v40, v41
	v_permlane16_swap_b32_e32 v42, v43
	global_store_dwordx4 v[252:253], v[40:43], off
	s_mov_b64 s[100:101], 0x28000
	v_lshl_add_u64 v[252:253], v[252:253], 0, s[100:101]
	s_mov_b64 s[100:101], 0x8000
	v_pk_add_f32 v[24:25], v[108:109], v[12:13]
	v_pk_add_f32 v[26:27], v[110:111], v[14:15]
	v_pk_add_f32 v[28:29], v[104:105], v[8:9]
	v_pk_add_f32 v[30:31], v[106:107], v[10:11]
	v_pk_add_f32 v[32:33], v[76:77], v[4:5]
	v_pk_add_f32 v[34:35], v[78:79], v[6:7]
	v_pk_add_f32 v[36:37], v[72:73], v[0:1]
	v_pk_add_f32 v[38:39], v[74:75], v[2:3]
	v_med3_f32 v24, v24, s77, v200
	v_med3_f32 v25, v25, s77, v200
	v_med3_f32 v26, v26, s77, v200
	v_med3_f32 v27, v27, s77, v200
	v_med3_f32 v28, v28, s77, v200
	v_med3_f32 v29, v29, s77, v200
	v_med3_f32 v30, v30, s77, v200
	v_med3_f32 v31, v31, s77, v200
	v_med3_f32 v32, v32, s77, v200
	v_med3_f32 v33, v33, s77, v200
	v_med3_f32 v34, v34, s77, v200
	v_med3_f32 v35, v35, s77, v200
	v_med3_f32 v36, v36, s77, v200
	v_med3_f32 v37, v37, s77, v200
	v_med3_f32 v38, v38, s77, v200
	v_med3_f32 v39, v39, s77, v200
	v_cvt_pk_fp8_f32 v20, v24, v25
	v_cvt_pk_fp8_f32 v21, v28, v29
	v_cvt_pk_fp8_f32 v22, v32, v33
	v_cvt_pk_fp8_f32 v23, v36, v37
	v_cvt_pk_fp8_f32 v20, v26, v27 op_sel:[0,0,1]
	v_cvt_pk_fp8_f32 v21, v30, v31 op_sel:[0,0,1]
	v_cvt_pk_fp8_f32 v22, v34, v35 op_sel:[0,0,1]
	v_cvt_pk_fp8_f32 v23, v38, v39 op_sel:[0,0,1]
	s_nop 1
	v_permlane32_swap_b32_e32 v20, v22
	v_permlane32_swap_b32_e32 v21, v23
	s_nop 1
	v_permlane16_swap_b32_e32 v20, v21
	v_permlane16_swap_b32_e32 v22, v23
	global_store_dwordx4 v[252:253], v[20:23], off
	v_lshl_add_u64 v[252:253], v[252:253], 0, s[100:101]
	v_pk_add_f32 v[24:25], v[100:101], v[12:13]
	v_pk_add_f32 v[26:27], v[102:103], v[14:15]
	v_pk_add_f32 v[28:29], v[96:97], v[8:9]
	v_pk_add_f32 v[30:31], v[98:99], v[10:11]
	v_pk_add_f32 v[32:33], v[68:69], v[4:5]
	v_pk_add_f32 v[34:35], v[70:71], v[6:7]
	v_pk_add_f32 v[36:37], v[64:65], v[0:1]
	v_pk_add_f32 v[38:39], v[66:67], v[2:3]
	v_med3_f32 v24, v24, s77, v200
	v_med3_f32 v25, v25, s77, v200
	v_med3_f32 v26, v26, s77, v200
	v_med3_f32 v27, v27, s77, v200
	v_med3_f32 v28, v28, s77, v200
	v_med3_f32 v29, v29, s77, v200
	v_med3_f32 v30, v30, s77, v200
	v_med3_f32 v31, v31, s77, v200
	v_med3_f32 v32, v32, s77, v200
	v_med3_f32 v33, v33, s77, v200
	v_med3_f32 v34, v34, s77, v200
	v_med3_f32 v35, v35, s77, v200
	v_med3_f32 v36, v36, s77, v200
	v_med3_f32 v37, v37, s77, v200
	v_med3_f32 v38, v38, s77, v200
	v_med3_f32 v39, v39, s77, v200
	v_cvt_pk_fp8_f32 v40, v24, v25
	v_cvt_pk_fp8_f32 v41, v28, v29
	v_cvt_pk_fp8_f32 v42, v32, v33
	v_cvt_pk_fp8_f32 v43, v36, v37
	v_cvt_pk_fp8_f32 v40, v26, v27 op_sel:[0,0,1]
	v_cvt_pk_fp8_f32 v41, v30, v31 op_sel:[0,0,1]
	v_cvt_pk_fp8_f32 v42, v34, v35 op_sel:[0,0,1]
	v_cvt_pk_fp8_f32 v43, v38, v39 op_sel:[0,0,1]
	s_nop 1
	v_permlane32_swap_b32_e32 v40, v42
	v_permlane32_swap_b32_e32 v41, v43
	s_nop 1
	v_permlane16_swap_b32_e32 v40, v41
	v_permlane16_swap_b32_e32 v42, v43
	global_store_dwordx4 v[252:253], v[40:43], off
	v_lshl_add_u64 v[252:253], v[252:253], 0, s[100:101]
	v_pk_add_f32 v[24:25], v[92:93], v[12:13]
	v_pk_add_f32 v[26:27], v[94:95], v[14:15]
	v_pk_add_f32 v[28:29], v[88:89], v[8:9]
	v_pk_add_f32 v[30:31], v[90:91], v[10:11]
	v_pk_add_f32 v[32:33], v[60:61], v[4:5]
	v_pk_add_f32 v[34:35], v[62:63], v[6:7]
	v_pk_add_f32 v[36:37], v[56:57], v[0:1]
	v_pk_add_f32 v[38:39], v[58:59], v[2:3]
	v_med3_f32 v24, v24, s77, v200
	v_med3_f32 v25, v25, s77, v200
	v_med3_f32 v26, v26, s77, v200
	v_med3_f32 v27, v27, s77, v200
	v_med3_f32 v28, v28, s77, v200
	v_med3_f32 v29, v29, s77, v200
	v_med3_f32 v30, v30, s77, v200
	v_med3_f32 v31, v31, s77, v200
	v_med3_f32 v32, v32, s77, v200
	v_med3_f32 v33, v33, s77, v200
	v_med3_f32 v34, v34, s77, v200
	v_med3_f32 v35, v35, s77, v200
	v_med3_f32 v36, v36, s77, v200
	v_med3_f32 v37, v37, s77, v200
	v_med3_f32 v38, v38, s77, v200
	v_med3_f32 v39, v39, s77, v200
	v_cvt_pk_fp8_f32 v20, v24, v25
	v_cvt_pk_fp8_f32 v21, v28, v29
	v_cvt_pk_fp8_f32 v22, v32, v33
	v_cvt_pk_fp8_f32 v23, v36, v37
	v_cvt_pk_fp8_f32 v20, v26, v27 op_sel:[0,0,1]
	v_cvt_pk_fp8_f32 v21, v30, v31 op_sel:[0,0,1]
	v_cvt_pk_fp8_f32 v22, v34, v35 op_sel:[0,0,1]
	v_cvt_pk_fp8_f32 v23, v38, v39 op_sel:[0,0,1]
	s_nop 1
	v_permlane32_swap_b32_e32 v20, v22
	v_permlane32_swap_b32_e32 v21, v23
	s_nop 1
	v_permlane16_swap_b32_e32 v20, v21
	v_permlane16_swap_b32_e32 v22, v23
	global_store_dwordx4 v[252:253], v[20:23], off
	v_lshl_add_u64 v[252:253], v[252:253], 0, s[100:101]
	v_pk_add_f32 v[24:25], v[84:85], v[12:13]
	v_pk_add_f32 v[26:27], v[86:87], v[14:15]
	v_pk_add_f32 v[28:29], v[80:81], v[8:9]
	v_pk_add_f32 v[30:31], v[82:83], v[10:11]
	v_pk_add_f32 v[32:33], v[52:53], v[4:5]
	v_pk_add_f32 v[34:35], v[54:55], v[6:7]
	v_pk_add_f32 v[36:37], v[48:49], v[0:1]
	v_pk_add_f32 v[38:39], v[50:51], v[2:3]
	v_med3_f32 v24, v24, s77, v200
	v_med3_f32 v25, v25, s77, v200
	v_med3_f32 v26, v26, s77, v200
	v_med3_f32 v27, v27, s77, v200
	v_med3_f32 v28, v28, s77, v200
	v_med3_f32 v29, v29, s77, v200
	v_med3_f32 v30, v30, s77, v200
	v_med3_f32 v31, v31, s77, v200
	v_med3_f32 v32, v32, s77, v200
	v_med3_f32 v33, v33, s77, v200
	v_med3_f32 v34, v34, s77, v200
	v_med3_f32 v35, v35, s77, v200
	v_med3_f32 v36, v36, s77, v200
	v_med3_f32 v37, v37, s77, v200
	v_med3_f32 v38, v38, s77, v200
	v_med3_f32 v39, v39, s77, v200
	v_cvt_pk_fp8_f32 v40, v24, v25
	v_cvt_pk_fp8_f32 v41, v28, v29
	v_cvt_pk_fp8_f32 v42, v32, v33
	v_cvt_pk_fp8_f32 v43, v36, v37
	v_cvt_pk_fp8_f32 v40, v26, v27 op_sel:[0,0,1]
	v_cvt_pk_fp8_f32 v41, v30, v31 op_sel:[0,0,1]
	v_cvt_pk_fp8_f32 v42, v34, v35 op_sel:[0,0,1]
	v_cvt_pk_fp8_f32 v43, v38, v39 op_sel:[0,0,1]
	s_nop 1
	v_permlane32_swap_b32_e32 v40, v42
	v_permlane32_swap_b32_e32 v41, v43
	s_nop 1
	v_permlane16_swap_b32_e32 v40, v41
	v_permlane16_swap_b32_e32 v42, v43
	global_store_dwordx4 v[252:253], v[40:43], off
	s_cbranch_vccnz .LBB0_994
	v_mov_b32_e32 v48, 0
	s_mov_b32 s81, s79
	s_mov_b64 s[8:9], s[22:23]
	s_mov_b32 s6, s20
	s_mov_b32 s44, s82
	s_mov_b32 s10, s21
	s_mov_b32 s80, s71
	v_mov_b32_e32 v49, v48
	v_mov_b32_e32 v50, v48
	v_mov_b32_e32 v51, v48
	v_mov_b32_e32 v52, v48
	v_mov_b32_e32 v53, v48
	v_mov_b32_e32 v54, v48
	v_mov_b32_e32 v55, v48
	v_mov_b32_e32 v56, v48
	v_mov_b32_e32 v57, v48
	v_mov_b32_e32 v58, v48
	v_mov_b32_e32 v59, v48
	v_mov_b32_e32 v60, v48
	v_mov_b32_e32 v61, v48
	v_mov_b32_e32 v62, v48
	v_mov_b32_e32 v63, v48
	v_mov_b32_e32 v64, v48
	v_mov_b32_e32 v65, v48
	v_mov_b32_e32 v66, v48
	v_mov_b32_e32 v67, v48
	v_mov_b32_e32 v68, v48
	v_mov_b32_e32 v69, v48
	v_mov_b32_e32 v70, v48
	v_mov_b32_e32 v71, v48
	v_mov_b32_e32 v72, v48
	v_mov_b32_e32 v73, v48
	v_mov_b32_e32 v74, v48
	v_mov_b32_e32 v75, v48
	v_mov_b32_e32 v76, v48
	v_mov_b32_e32 v77, v48
	v_mov_b32_e32 v78, v48
	v_mov_b32_e32 v79, v48
	v_mov_b32_e32 v80, v48
	v_mov_b32_e32 v81, v48
	v_mov_b32_e32 v82, v48
	v_mov_b32_e32 v83, v48
	v_mov_b32_e32 v84, v48
	v_mov_b32_e32 v85, v48
	v_mov_b32_e32 v86, v48
	v_mov_b32_e32 v87, v48
	v_mov_b32_e32 v88, v48
	v_mov_b32_e32 v89, v48
	v_mov_b32_e32 v90, v48
	v_mov_b32_e32 v91, v48
	v_mov_b32_e32 v92, v48
	v_mov_b32_e32 v93, v48
	v_mov_b32_e32 v94, v48
	v_mov_b32_e32 v95, v48
	v_mov_b32_e32 v96, v48
	v_mov_b32_e32 v97, v48
	v_mov_b32_e32 v98, v48
	v_mov_b32_e32 v99, v48
	v_mov_b32_e32 v100, v48
	v_mov_b32_e32 v101, v48
	v_mov_b32_e32 v102, v48
	v_mov_b32_e32 v103, v48
	v_mov_b32_e32 v104, v48
	v_mov_b32_e32 v105, v48
	v_mov_b32_e32 v106, v48
	v_mov_b32_e32 v107, v48
	v_mov_b32_e32 v108, v48
	v_mov_b32_e32 v109, v48
	v_mov_b32_e32 v110, v48
	v_mov_b32_e32 v111, v48
	v_mov_b32_e32 v112, v48
	v_mov_b32_e32 v113, v48
	v_mov_b32_e32 v114, v48
	v_mov_b32_e32 v115, v48
	v_mov_b32_e32 v116, v48
	v_mov_b32_e32 v117, v48
	v_mov_b32_e32 v118, v48
	v_mov_b32_e32 v119, v48
	v_mov_b32_e32 v120, v48
	v_mov_b32_e32 v121, v48
	v_mov_b32_e32 v122, v48
	v_mov_b32_e32 v123, v48
	v_mov_b32_e32 v124, v48
	v_mov_b32_e32 v125, v48
	v_mov_b32_e32 v126, v48
	v_mov_b32_e32 v127, v48
	v_mov_b32_e32 v128, v48
	v_mov_b32_e32 v129, v48
	v_mov_b32_e32 v130, v48
	v_mov_b32_e32 v131, v48
	v_mov_b32_e32 v132, v48
	v_mov_b32_e32 v133, v48
	v_mov_b32_e32 v134, v48
	v_mov_b32_e32 v135, v48
	v_mov_b32_e32 v136, v48
	v_mov_b32_e32 v137, v48
	v_mov_b32_e32 v138, v48
	v_mov_b32_e32 v139, v48
	v_mov_b32_e32 v140, v48
	v_mov_b32_e32 v141, v48
	v_mov_b32_e32 v142, v48
	v_mov_b32_e32 v143, v48
	v_mov_b32_e32 v144, v48
	v_mov_b32_e32 v145, v48
	v_mov_b32_e32 v146, v48
	v_mov_b32_e32 v147, v48
	v_mov_b32_e32 v148, v48
	v_mov_b32_e32 v149, v48
	v_mov_b32_e32 v150, v48
	v_mov_b32_e32 v151, v48
	v_mov_b32_e32 v152, v48
	v_mov_b32_e32 v153, v48
	v_mov_b32_e32 v154, v48
	v_mov_b32_e32 v155, v48
	v_mov_b32_e32 v156, v48
	v_mov_b32_e32 v157, v48
	v_mov_b32_e32 v158, v48
	v_mov_b32_e32 v159, v48
	v_mov_b32_e32 v160, v48
	v_mov_b32_e32 v161, v48
	v_mov_b32_e32 v162, v48
	v_mov_b32_e32 v163, v48
	v_mov_b32_e32 v164, v48
	v_mov_b32_e32 v165, v48
	v_mov_b32_e32 v166, v48
	v_mov_b32_e32 v167, v48
	v_mov_b32_e32 v168, v48
	v_mov_b32_e32 v169, v48
	v_mov_b32_e32 v170, v48
	v_mov_b32_e32 v171, v48
	v_mov_b32_e32 v172, v48
	v_mov_b32_e32 v173, v48
	v_mov_b32_e32 v174, v48
	v_mov_b32_e32 v175, v48
	s_branch .LBB0_994
